# MoE K-loops: next even-half A-tile DMA addresses precomputed inside the odd half's MFMA segment; first two LDS-DMA loads issue right after the back-edge barrier
# speedup vs baseline: 1.0327x; 1.0025x over previous
.LBB0_732:
	s_cmp_lg_u64 s[2:3], 0
	s_cbranch_scc1 .Lswp_guO_half
	ds_read_b64_tr_b16 v[162:163], v190 offset:32768
	ds_read_b64_tr_b16 v[164:165], v191 offset:32768
	ds_read_b64_tr_b16 v[170:171], v192 offset:32768
	ds_read_b64_tr_b16 v[172:173], v193 offset:32768
	ds_read_b128 v[214:217], v207 offset:32768
	ds_read_b128 v[224:227], v207 offset:34816
	ds_read_b128 v[232:235], v207 offset:36864
	ds_read_b128 v[240:243], v207 offset:38912
	ds_read_b64_tr_b16 v[166:167], v190 offset:40960
	ds_read_b64_tr_b16 v[168:169], v191 offset:40960
	ds_read_b64_tr_b16 v[174:175], v192 offset:40960
	ds_read_b64_tr_b16 v[176:177], v193 offset:40960
	ds_read_b128 v[218:221], v207 offset:33792
	ds_read_b128 v[228:231], v207 offset:35840
	ds_read_b128 v[236:239], v207 offset:37888
	ds_read_b128 v[244:247], v207 offset:39936
	s_lshl_b64 s[2:3], s[38:39], 18
	s_add_u32 s4, s2, 0x40000
	s_addc_u32 s5, s3, 0
	s_add_u32 s2, s67, s4
	s_addc_u32 s3, s66, s5
	s_add_u32 s4, s35, s4
	s_addc_u32 s5, s34, s5
	s_add_i32 s94, s17, 2
	s_ashr_i32 s95, s94, 31
	s_lshl_b64 s[94:95], s[94:95], 7
	s_add_u32 s94, s8, s94
	s_addc_u32 s95, s9, s95
	s_add_u32 s94, s94, 0x80
	s_addc_u32 s95, s95, 0
	v_lshl_add_u64 v[250:251], s[94:95], 0, v[178:179]
	v_lshl_add_u64 v[252:253], s[94:95], 0, v[180:181]
	s_setprio 1
	s_waitcnt lgkmcnt(11)
	v_mfma_f32_16x16x32_bf16 v[158:161], v[162:165], v[214:217], v[158:161]
	v_mfma_f32_16x16x32_bf16 v[154:157], v[170:173], v[214:217], v[154:157]
	ds_read_b128 v[214:217], v207 offset:49152
	s_waitcnt lgkmcnt(11)
	v_mfma_f32_16x16x32_bf16 v[146:149], v[162:165], v[224:227], v[146:149]
	v_mfma_f32_16x16x32_bf16 v[138:141], v[170:173], v[224:227], v[138:141]
	ds_read_b128 v[224:227], v207 offset:51200
	s_waitcnt lgkmcnt(11)
	v_mfma_f32_16x16x32_bf16 v[130:133], v[162:165], v[232:235], v[130:133]
	v_mfma_f32_16x16x32_bf16 v[122:125], v[170:173], v[232:235], v[122:125]
	ds_read_b128 v[232:235], v207 offset:53248
	s_waitcnt lgkmcnt(11)
	v_mfma_f32_16x16x32_bf16 v[114:117], v[162:165], v[240:243], v[114:117]
	v_mfma_f32_16x16x32_bf16 v[106:109], v[170:173], v[240:243], v[106:109]
	ds_read_b128 v[240:243], v207 offset:55296
	s_waitcnt lgkmcnt(7)
	v_mfma_f32_16x16x32_bf16 v[158:161], v[166:169], v[218:221], v[158:161]
	v_mfma_f32_16x16x32_bf16 v[154:157], v[174:177], v[218:221], v[154:157]
	ds_read_b128 v[218:221], v207 offset:50176
	s_waitcnt lgkmcnt(7)
	v_mfma_f32_16x16x32_bf16 v[146:149], v[166:169], v[228:231], v[146:149]
	v_mfma_f32_16x16x32_bf16 v[138:141], v[174:177], v[228:231], v[138:141]
	ds_read_b128 v[228:231], v207 offset:52224
	s_waitcnt lgkmcnt(7)
	v_mfma_f32_16x16x32_bf16 v[130:133], v[166:169], v[236:239], v[130:133]
	v_mfma_f32_16x16x32_bf16 v[122:125], v[174:177], v[236:239], v[122:125]
	ds_read_b128 v[236:239], v207 offset:54272
	s_waitcnt lgkmcnt(7)
	v_mfma_f32_16x16x32_bf16 v[114:117], v[166:169], v[244:247], v[114:117]
	v_mfma_f32_16x16x32_bf16 v[106:109], v[174:177], v[244:247], v[106:109]
	ds_read_b128 v[244:247], v207 offset:56320
	s_waitcnt lgkmcnt(7)
	v_mfma_f32_16x16x32_bf16 v[94:97], v[162:165], v[214:217], v[94:97]
	v_mfma_f32_16x16x32_bf16 v[86:89], v[170:173], v[214:217], v[86:89]
	ds_read_b128 v[214:217], v207 offset:32768
	s_waitcnt lgkmcnt(7)
	v_mfma_f32_16x16x32_bf16 v[78:81], v[162:165], v[224:227], v[78:81]
	v_mfma_f32_16x16x32_bf16 v[70:73], v[170:173], v[224:227], v[70:73]
	ds_read_b128 v[224:227], v207 offset:34816
	s_waitcnt lgkmcnt(7)
	v_mfma_f32_16x16x32_bf16 v[62:65], v[162:165], v[232:235], v[62:65]
	v_mfma_f32_16x16x32_bf16 v[54:57], v[170:173], v[232:235], v[54:57]
	ds_read_b128 v[232:235], v207 offset:36864
	s_waitcnt lgkmcnt(7)
	v_mfma_f32_16x16x32_bf16 v[46:49], v[162:165], v[240:243], v[46:49]
	v_mfma_f32_16x16x32_bf16 v[38:41], v[170:173], v[240:243], v[38:41]
	ds_read_b128 v[240:243], v207 offset:38912
	ds_read_b64_tr_b16 v[162:163], v190 offset:49152
	ds_read_b64_tr_b16 v[164:165], v191 offset:49152
	ds_read_b64_tr_b16 v[170:171], v192 offset:49152
	ds_read_b64_tr_b16 v[172:173], v193 offset:49152
	s_waitcnt lgkmcnt(11)
	v_mfma_f32_16x16x32_bf16 v[94:97], v[166:169], v[218:221], v[94:97]
	v_mfma_f32_16x16x32_bf16 v[86:89], v[174:177], v[218:221], v[86:89]
	ds_read_b128 v[218:221], v207 offset:33792
	s_waitcnt lgkmcnt(11)
	v_mfma_f32_16x16x32_bf16 v[78:81], v[166:169], v[228:231], v[78:81]
	v_mfma_f32_16x16x32_bf16 v[70:73], v[174:177], v[228:231], v[70:73]
	ds_read_b128 v[228:231], v207 offset:35840
	s_waitcnt lgkmcnt(11)
	v_mfma_f32_16x16x32_bf16 v[62:65], v[166:169], v[236:239], v[62:65]
	v_mfma_f32_16x16x32_bf16 v[54:57], v[174:177], v[236:239], v[54:57]
	ds_read_b128 v[236:239], v207 offset:37888
	s_waitcnt lgkmcnt(11)
	v_mfma_f32_16x16x32_bf16 v[46:49], v[166:169], v[244:247], v[46:49]
	v_mfma_f32_16x16x32_bf16 v[38:41], v[174:177], v[244:247], v[38:41]
	ds_read_b128 v[244:247], v207 offset:39936
	ds_read_b64_tr_b16 v[166:167], v190 offset:57344
	ds_read_b64_tr_b16 v[168:169], v191 offset:57344
	ds_read_b64_tr_b16 v[174:175], v192 offset:57344
	ds_read_b64_tr_b16 v[176:177], v193 offset:57344
	s_waitcnt lgkmcnt(8)
	v_mfma_f32_16x16x32_bf16 v[150:153], v[162:165], v[214:217], v[150:153]
	v_mfma_f32_16x16x32_bf16 v[142:145], v[170:173], v[214:217], v[142:145]
	ds_read_b128 v[214:217], v207 offset:49152
	v_mfma_f32_16x16x32_bf16 v[134:137], v[162:165], v[224:227], v[134:137]
	v_mfma_f32_16x16x32_bf16 v[126:129], v[170:173], v[224:227], v[126:129]
	ds_read_b128 v[224:227], v207 offset:51200
	v_mfma_f32_16x16x32_bf16 v[118:121], v[162:165], v[232:235], v[118:121]
	v_mfma_f32_16x16x32_bf16 v[110:113], v[170:173], v[232:235], v[110:113]
	ds_read_b128 v[232:235], v207 offset:53248
	v_mfma_f32_16x16x32_bf16 v[102:105], v[162:165], v[240:243], v[102:105]
	v_mfma_f32_16x16x32_bf16 v[98:101], v[170:173], v[240:243], v[98:101]
	ds_read_b128 v[240:243], v207 offset:55296
	s_waitcnt lgkmcnt(4)
	v_mfma_f32_16x16x32_bf16 v[150:153], v[166:169], v[218:221], v[150:153]
	v_mfma_f32_16x16x32_bf16 v[142:145], v[174:177], v[218:221], v[142:145]
	ds_read_b128 v[218:221], v207 offset:50176
	v_mfma_f32_16x16x32_bf16 v[134:137], v[166:169], v[228:231], v[134:137]
	v_mfma_f32_16x16x32_bf16 v[126:129], v[174:177], v[228:231], v[126:129]
	ds_read_b128 v[228:231], v207 offset:52224
	v_mfma_f32_16x16x32_bf16 v[118:121], v[166:169], v[236:239], v[118:121]
	v_mfma_f32_16x16x32_bf16 v[110:113], v[174:177], v[236:239], v[110:113]
	ds_read_b128 v[236:239], v207 offset:54272
	v_mfma_f32_16x16x32_bf16 v[102:105], v[166:169], v[244:247], v[102:105]
	v_mfma_f32_16x16x32_bf16 v[98:101], v[174:177], v[244:247], v[98:101]
	ds_read_b128 v[244:247], v207 offset:56320
	s_waitcnt lgkmcnt(7)
	v_mfma_f32_16x16x32_bf16 v[90:93], v[162:165], v[214:217], v[90:93]
	v_mfma_f32_16x16x32_bf16 v[82:85], v[170:173], v[214:217], v[82:85]
	s_waitcnt vmcnt(9)
	v_cvt_pk_bf16_f32 v248, v2, v3
	v_cvt_pk_bf16_f32 v249, v4, v5
	ds_write_b64 v197, v[248:249] offset:16384
	global_load_dwordx4 v[2:5], v189, s[2:3]
	s_waitcnt lgkmcnt(7)
	v_mfma_f32_16x16x32_bf16 v[74:77], v[162:165], v[224:227], v[74:77]
	v_mfma_f32_16x16x32_bf16 v[66:69], v[170:173], v[224:227], v[66:69]
	s_waitcnt vmcnt(9)
	v_cvt_pk_bf16_f32 v248, v6, v7
	v_cvt_pk_bf16_f32 v249, v8, v9
	ds_write_b64 v196, v[248:249] offset:16384
	global_load_dwordx4 v[6:9], v189, s[4:5]
	s_waitcnt lgkmcnt(7)
	v_mfma_f32_16x16x32_bf16 v[58:61], v[162:165], v[232:235], v[58:61]
	v_mfma_f32_16x16x32_bf16 v[50:53], v[170:173], v[232:235], v[50:53]
	s_waitcnt vmcnt(9)
	v_cvt_pk_bf16_f32 v248, v10, v11
	v_cvt_pk_bf16_f32 v249, v12, v13
	ds_write_b64 v197, v[248:249]
	s_add_u32 s98, s2, 0x2000
	s_addc_u32 s99, s3, 0
	global_load_dwordx4 v[10:13], v189, s[98:99]
	s_waitcnt lgkmcnt(7)
	v_mfma_f32_16x16x32_bf16 v[42:45], v[162:165], v[240:243], v[42:45]
	v_mfma_f32_16x16x32_bf16 v[30:33], v[170:173], v[240:243], v[30:33]
	s_waitcnt vmcnt(9)
	v_cvt_pk_bf16_f32 v248, v14, v15
	v_cvt_pk_bf16_f32 v249, v16, v17
	ds_write_b64 v195, v[248:249] offset:16384
	s_add_u32 s100, s4, 0x2000
	s_addc_u32 s101, s5, 0
	global_load_dwordx4 v[14:17], v189, s[100:101]
	s_waitcnt lgkmcnt(7)
	v_mfma_f32_16x16x32_bf16 v[90:93], v[166:169], v[218:221], v[90:93]
	v_mfma_f32_16x16x32_bf16 v[82:85], v[174:177], v[218:221], v[82:85]
	s_waitcnt vmcnt(9)
	v_cvt_pk_bf16_f32 v248, v18, v19
	v_cvt_pk_bf16_f32 v249, v20, v21
	ds_write_b64 v196, v[248:249]
	s_add_u32 s98, s2, 0x4000
	s_addc_u32 s99, s3, 0
	global_load_dwordx4 v[18:21], v189, s[98:99]
	s_waitcnt lgkmcnt(7)
	v_mfma_f32_16x16x32_bf16 v[74:77], v[166:169], v[228:231], v[74:77]
	v_mfma_f32_16x16x32_bf16 v[66:69], v[174:177], v[228:231], v[66:69]
	s_waitcnt vmcnt(9)
	v_cvt_pk_bf16_f32 v248, v22, v23
	v_cvt_pk_bf16_f32 v249, v24, v25
	ds_write_b64 v194, v[248:249] offset:16384
	s_add_u32 s100, s4, 0x4000
	s_addc_u32 s101, s5, 0
	global_load_dwordx4 v[22:25], v189, s[100:101]
	s_waitcnt lgkmcnt(7)
	v_mfma_f32_16x16x32_bf16 v[58:61], v[166:169], v[236:239], v[58:61]
	v_mfma_f32_16x16x32_bf16 v[50:53], v[174:177], v[236:239], v[50:53]
	s_waitcnt vmcnt(9)
	v_cvt_pk_bf16_f32 v248, v26, v27
	v_cvt_pk_bf16_f32 v249, v28, v29
	ds_write_b64 v195, v[248:249]
	s_add_u32 s98, s2, 0x6000
	s_addc_u32 s99, s3, 0
	global_load_dwordx4 v[26:29], v189, s[98:99]
	s_waitcnt lgkmcnt(7)
	v_mfma_f32_16x16x32_bf16 v[42:45], v[166:169], v[244:247], v[42:45]
	v_mfma_f32_16x16x32_bf16 v[30:33], v[174:177], v[244:247], v[30:33]
	s_waitcnt vmcnt(9)
	v_cvt_pk_bf16_f32 v248, v34, v35
	v_cvt_pk_bf16_f32 v249, v36, v37
	ds_write_b64 v194, v[248:249]
	s_add_u32 s100, s4, 0x6000
	s_addc_u32 s101, s5, 0
	global_load_dwordx4 v[34:37], v189, s[100:101]
	s_setprio 0
.LBB0_736:
.Lswp_guO_tail:
	s_add_i32 m0, s51, 0x8000
	s_waitcnt vmcnt(8)
	s_waitcnt lgkmcnt(0)
	s_barrier
	s_cmp_gt_u32 s17, 29
	s_cbranch_scc1 .LBB0_738
	global_load_lds_dwordx4 v[250:251], off
	s_add_i32 m0, s51, 0xa000
	s_mov_b32 s34, s17
	global_load_lds_dwordx4 v[252:253], off
	s_add_i32 s17, s34, 2
	s_mov_b32 s4, s17
	s_ashr_i32 s5, s4, 31
	s_mov_b64 s[38:39], s[94:95]
	s_andn2_b64 vcc, exec, s[0:1]
	v_cndmask_b32_e64 v162, 0, 1, s[0:1]
	v_cmp_ne_u32_e64 s[2:3], 1, v162
	s_cbranch_vccnz .LBB0_726
	v_lshl_add_u64 v[164:165], s[38:39], 0, v[182:183]
	s_add_i32 m0, s51, 0xc000
	v_lshl_add_u64 v[162:163], s[38:39], 0, v[184:185]
	global_load_lds_dwordx4 v[164:165], off
	s_add_i32 m0, s51, 0xe000
	s_nop 0
	global_load_lds_dwordx4 v[162:163], off
	s_branch .LBB0_726

.Lswp_guO_half:
	ds_read_b64_tr_b16 v[162:163], v190 offset:32768
	ds_read_b64_tr_b16 v[164:165], v191 offset:32768
	ds_read_b64_tr_b16 v[170:171], v192 offset:32768
	ds_read_b64_tr_b16 v[172:173], v193 offset:32768
	ds_read_b128 v[214:217], v207 offset:32768
	ds_read_b128 v[224:227], v207 offset:34816
	ds_read_b128 v[232:235], v207 offset:36864
	ds_read_b128 v[240:243], v207 offset:38912
	ds_read_b64_tr_b16 v[166:167], v190 offset:40960
	ds_read_b64_tr_b16 v[168:169], v191 offset:40960
	ds_read_b64_tr_b16 v[174:175], v192 offset:40960
	ds_read_b64_tr_b16 v[176:177], v193 offset:40960
	ds_read_b128 v[218:221], v207 offset:33792
	ds_read_b128 v[228:231], v207 offset:35840
	ds_read_b128 v[236:239], v207 offset:37888
	ds_read_b128 v[244:247], v207 offset:39936
	s_lshl_b64 s[2:3], s[38:39], 18
	s_add_u32 s4, s2, 0x40000
	s_addc_u32 s5, s3, 0
	s_add_u32 s2, s67, s4
	s_addc_u32 s3, s66, s5
	s_add_u32 s4, s35, s4
	s_addc_u32 s5, s34, s5
	s_add_i32 s94, s17, 2
	s_ashr_i32 s95, s94, 31
	s_lshl_b64 s[94:95], s[94:95], 7
	s_add_u32 s94, s8, s94
	s_addc_u32 s95, s9, s95
	s_add_u32 s94, s94, 0x80
	s_addc_u32 s95, s95, 0
	v_lshl_add_u64 v[250:251], s[94:95], 0, v[178:179]
	v_lshl_add_u64 v[252:253], s[94:95], 0, v[180:181]
	s_setprio 1
	s_waitcnt lgkmcnt(11)
	v_mfma_f32_16x16x32_bf16 v[158:161], v[162:165], v[214:217], v[158:161]
	v_mfma_f32_16x16x32_bf16 v[154:157], v[170:173], v[214:217], v[154:157]
	ds_read_b128 v[214:217], v207 offset:32768
	s_waitcnt lgkmcnt(11)
	v_mfma_f32_16x16x32_bf16 v[146:149], v[162:165], v[224:227], v[146:149]
	v_mfma_f32_16x16x32_bf16 v[138:141], v[170:173], v[224:227], v[138:141]
	ds_read_b128 v[224:227], v207 offset:34816
	s_waitcnt lgkmcnt(11)
	v_mfma_f32_16x16x32_bf16 v[130:133], v[162:165], v[232:235], v[130:133]
	v_mfma_f32_16x16x32_bf16 v[122:125], v[170:173], v[232:235], v[122:125]
	ds_read_b128 v[232:235], v207 offset:36864
	s_waitcnt lgkmcnt(11)
	v_mfma_f32_16x16x32_bf16 v[114:117], v[162:165], v[240:243], v[114:117]
	v_mfma_f32_16x16x32_bf16 v[106:109], v[170:173], v[240:243], v[106:109]
	ds_read_b128 v[240:243], v207 offset:38912
	ds_read_b64_tr_b16 v[162:163], v190 offset:49152
	ds_read_b64_tr_b16 v[164:165], v191 offset:49152
	ds_read_b64_tr_b16 v[170:171], v192 offset:49152
	ds_read_b64_tr_b16 v[172:173], v193 offset:49152
	s_waitcnt lgkmcnt(11)
	v_mfma_f32_16x16x32_bf16 v[158:161], v[166:169], v[218:221], v[158:161]
	v_mfma_f32_16x16x32_bf16 v[154:157], v[174:177], v[218:221], v[154:157]
	ds_read_b128 v[218:221], v207 offset:33792
	s_waitcnt lgkmcnt(11)
	v_mfma_f32_16x16x32_bf16 v[146:149], v[166:169], v[228:231], v[146:149]
	v_mfma_f32_16x16x32_bf16 v[138:141], v[174:177], v[228:231], v[138:141]
	ds_read_b128 v[228:231], v207 offset:35840
	s_waitcnt lgkmcnt(11)
	v_mfma_f32_16x16x32_bf16 v[130:133], v[166:169], v[236:239], v[130:133]
	v_mfma_f32_16x16x32_bf16 v[122:125], v[174:177], v[236:239], v[122:125]
	ds_read_b128 v[236:239], v207 offset:37888
	s_waitcnt lgkmcnt(11)
	v_mfma_f32_16x16x32_bf16 v[114:117], v[166:169], v[244:247], v[114:117]
	v_mfma_f32_16x16x32_bf16 v[106:109], v[174:177], v[244:247], v[106:109]
	ds_read_b128 v[244:247], v207 offset:39936
	ds_read_b64_tr_b16 v[166:167], v190 offset:57344
	ds_read_b64_tr_b16 v[168:169], v191 offset:57344
	ds_read_b64_tr_b16 v[174:175], v192 offset:57344
	ds_read_b64_tr_b16 v[176:177], v193 offset:57344
	s_waitcnt lgkmcnt(8)
	v_mfma_f32_16x16x32_bf16 v[150:153], v[162:165], v[214:217], v[150:153]
	v_mfma_f32_16x16x32_bf16 v[142:145], v[170:173], v[214:217], v[142:145]
	s_waitcnt vmcnt(9)
	v_cvt_pk_bf16_f32 v248, v2, v3
	v_cvt_pk_bf16_f32 v249, v4, v5
	ds_write_b64 v197, v[248:249] offset:16384
	global_load_dwordx4 v[2:5], v189, s[2:3]
	v_mfma_f32_16x16x32_bf16 v[134:137], v[162:165], v[224:227], v[134:137]
	v_mfma_f32_16x16x32_bf16 v[126:129], v[170:173], v[224:227], v[126:129]
	s_waitcnt vmcnt(9)
	v_cvt_pk_bf16_f32 v248, v6, v7
	v_cvt_pk_bf16_f32 v249, v8, v9
	ds_write_b64 v196, v[248:249] offset:16384
	global_load_dwordx4 v[6:9], v189, s[4:5]
	v_mfma_f32_16x16x32_bf16 v[118:121], v[162:165], v[232:235], v[118:121]
	v_mfma_f32_16x16x32_bf16 v[110:113], v[170:173], v[232:235], v[110:113]
	s_waitcnt vmcnt(9)
	v_cvt_pk_bf16_f32 v248, v10, v11
	v_cvt_pk_bf16_f32 v249, v12, v13
	ds_write_b64 v197, v[248:249]
	s_add_u32 s98, s2, 0x2000
	s_addc_u32 s99, s3, 0
	global_load_dwordx4 v[10:13], v189, s[98:99]
	v_mfma_f32_16x16x32_bf16 v[102:105], v[162:165], v[240:243], v[102:105]
	v_mfma_f32_16x16x32_bf16 v[98:101], v[170:173], v[240:243], v[98:101]
	s_waitcnt vmcnt(9)
	v_cvt_pk_bf16_f32 v248, v14, v15
	v_cvt_pk_bf16_f32 v249, v16, v17
	ds_write_b64 v195, v[248:249] offset:16384
	s_add_u32 s100, s4, 0x2000
	s_addc_u32 s101, s5, 0
	global_load_dwordx4 v[14:17], v189, s[100:101]
	s_waitcnt lgkmcnt(4)
	v_mfma_f32_16x16x32_bf16 v[150:153], v[166:169], v[218:221], v[150:153]
	v_mfma_f32_16x16x32_bf16 v[142:145], v[174:177], v[218:221], v[142:145]
	s_waitcnt vmcnt(9)
	v_cvt_pk_bf16_f32 v248, v18, v19
	v_cvt_pk_bf16_f32 v249, v20, v21
	ds_write_b64 v196, v[248:249]
	s_add_u32 s98, s2, 0x4000
	s_addc_u32 s99, s3, 0
	global_load_dwordx4 v[18:21], v189, s[98:99]
	v_mfma_f32_16x16x32_bf16 v[134:137], v[166:169], v[228:231], v[134:137]
	v_mfma_f32_16x16x32_bf16 v[126:129], v[174:177], v[228:231], v[126:129]
	s_waitcnt vmcnt(9)
	v_cvt_pk_bf16_f32 v248, v22, v23
	v_cvt_pk_bf16_f32 v249, v24, v25
	ds_write_b64 v194, v[248:249] offset:16384
	s_add_u32 s100, s4, 0x4000
	s_addc_u32 s101, s5, 0
	global_load_dwordx4 v[22:25], v189, s[100:101]
	v_mfma_f32_16x16x32_bf16 v[118:121], v[166:169], v[236:239], v[118:121]
	v_mfma_f32_16x16x32_bf16 v[110:113], v[174:177], v[236:239], v[110:113]
	s_waitcnt vmcnt(9)
	v_cvt_pk_bf16_f32 v248, v26, v27
	v_cvt_pk_bf16_f32 v249, v28, v29
	ds_write_b64 v195, v[248:249]
	s_add_u32 s98, s2, 0x6000
	s_addc_u32 s99, s3, 0
	global_load_dwordx4 v[26:29], v189, s[98:99]
	v_mfma_f32_16x16x32_bf16 v[102:105], v[166:169], v[244:247], v[102:105]
	v_mfma_f32_16x16x32_bf16 v[98:101], v[174:177], v[244:247], v[98:101]
	s_waitcnt vmcnt(9)
	v_cvt_pk_bf16_f32 v248, v34, v35
	v_cvt_pk_bf16_f32 v249, v36, v37
	ds_write_b64 v194, v[248:249]
	s_add_u32 s100, s4, 0x6000
	s_addc_u32 s101, s5, 0
	global_load_dwordx4 v[34:37], v189, s[100:101]
	s_setprio 0
	s_branch .Lswp_guO_tail

.LBB0_864:
	s_cmp_lg_u64 s[2:3], 0
	s_cbranch_scc1 .Lswp_dnO_half
	ds_read_b64_tr_b16 v[164:165], v190 offset:32768
	ds_read_b64_tr_b16 v[166:167], v191 offset:32768
	ds_read_b64_tr_b16 v[172:173], v192 offset:32768
	ds_read_b64_tr_b16 v[174:175], v193 offset:32768
	ds_read_b128 v[210:213], v207 offset:32768
	ds_read_b128 v[218:221], v207 offset:34816
	ds_read_b128 v[228:231], v207 offset:36864
	ds_read_b128 v[236:239], v207 offset:38912
	ds_read_b64_tr_b16 v[168:169], v190 offset:40960
	ds_read_b64_tr_b16 v[170:171], v191 offset:40960
	ds_read_b64_tr_b16 v[176:177], v192 offset:40960
	ds_read_b64_tr_b16 v[178:179], v193 offset:40960
	ds_read_b128 v[214:217], v207 offset:33792
	ds_read_b128 v[224:227], v207 offset:35840
	ds_read_b128 v[232:235], v207 offset:37888
	ds_read_b128 v[240:243], v207 offset:39936
	s_lshl_b64 s[2:3], s[48:49], 19
	s_add_u32 s48, s2, 0x80000
	s_addc_u32 s49, s3, 0
	s_add_u32 s2, s74, s48
	s_addc_u32 s3, s43, s49
	s_add_u32 s48, s37, s48
	s_addc_u32 s49, s35, s49
	s_add_i32 s94, s34, 2
	s_ashr_i32 s95, s94, 31
	s_lshl_b64 s[94:95], s[94:95], 7
	s_add_u32 s94, s22, s94
	s_addc_u32 s95, s23, s95
	s_add_u32 s94, s94, 0x80
	s_addc_u32 s95, s95, 0
	v_lshl_add_u64 v[250:251], s[94:95], 0, v[180:181]
	v_lshl_add_u64 v[252:253], s[94:95], 0, v[182:183]
	s_setprio 1
	s_waitcnt lgkmcnt(11)
	v_mfma_f32_16x16x32_bf16 v[160:163], v[164:167], v[210:213], v[160:163]
	v_mfma_f32_16x16x32_bf16 v[156:159], v[172:175], v[210:213], v[156:159]
	ds_read_b128 v[210:213], v207 offset:49152
	s_waitcnt lgkmcnt(11)
	v_mfma_f32_16x16x32_bf16 v[152:155], v[164:167], v[218:221], v[152:155]
	v_mfma_f32_16x16x32_bf16 v[148:151], v[172:175], v[218:221], v[148:151]
	ds_read_b128 v[218:221], v207 offset:51200
	s_waitcnt lgkmcnt(11)
	v_mfma_f32_16x16x32_bf16 v[136:139], v[164:167], v[228:231], v[136:139]
	v_mfma_f32_16x16x32_bf16 v[132:135], v[172:175], v[228:231], v[132:135]
	ds_read_b128 v[228:231], v207 offset:53248
	s_waitcnt lgkmcnt(11)
	v_mfma_f32_16x16x32_bf16 v[120:123], v[164:167], v[236:239], v[120:123]
	v_mfma_f32_16x16x32_bf16 v[116:119], v[172:175], v[236:239], v[116:119]
	ds_read_b128 v[236:239], v207 offset:55296
	s_waitcnt lgkmcnt(7)
	v_mfma_f32_16x16x32_bf16 v[160:163], v[168:171], v[214:217], v[160:163]
	v_mfma_f32_16x16x32_bf16 v[156:159], v[176:179], v[214:217], v[156:159]
	ds_read_b128 v[214:217], v207 offset:50176
	s_waitcnt lgkmcnt(7)
	v_mfma_f32_16x16x32_bf16 v[152:155], v[168:171], v[224:227], v[152:155]
	v_mfma_f32_16x16x32_bf16 v[148:151], v[176:179], v[224:227], v[148:151]
	ds_read_b128 v[224:227], v207 offset:52224
	s_waitcnt lgkmcnt(7)
	v_mfma_f32_16x16x32_bf16 v[136:139], v[168:171], v[232:235], v[136:139]
	v_mfma_f32_16x16x32_bf16 v[132:135], v[176:179], v[232:235], v[132:135]
	ds_read_b128 v[232:235], v207 offset:54272
	s_waitcnt lgkmcnt(7)
	v_mfma_f32_16x16x32_bf16 v[120:123], v[168:171], v[240:243], v[120:123]
	v_mfma_f32_16x16x32_bf16 v[116:119], v[176:179], v[240:243], v[116:119]
	ds_read_b128 v[240:243], v207 offset:56320
	s_waitcnt lgkmcnt(7)
	v_mfma_f32_16x16x32_bf16 v[80:83], v[164:167], v[210:213], v[80:83]
	v_mfma_f32_16x16x32_bf16 v[68:71], v[172:175], v[210:213], v[68:71]
	ds_read_b128 v[210:213], v207 offset:32768
	s_waitcnt lgkmcnt(7)
	v_mfma_f32_16x16x32_bf16 v[48:51], v[164:167], v[218:221], v[48:51]
	v_mfma_f32_16x16x32_bf16 v[44:47], v[172:175], v[218:221], v[44:47]
	ds_read_b128 v[218:221], v207 offset:34816
	s_waitcnt lgkmcnt(7)
	v_mfma_f32_16x16x32_bf16 v[32:35], v[164:167], v[228:231], v[32:35]
	v_mfma_f32_16x16x32_bf16 v[28:31], v[172:175], v[228:231], v[28:31]
	ds_read_b128 v[228:231], v207 offset:36864
	s_waitcnt lgkmcnt(7)
	v_mfma_f32_16x16x32_bf16 v[16:19], v[164:167], v[236:239], v[16:19]
	v_mfma_f32_16x16x32_bf16 v[12:15], v[172:175], v[236:239], v[12:15]
	ds_read_b128 v[236:239], v207 offset:38912
	ds_read_b64_tr_b16 v[164:165], v190 offset:49152
	ds_read_b64_tr_b16 v[166:167], v191 offset:49152
	ds_read_b64_tr_b16 v[172:173], v192 offset:49152
	ds_read_b64_tr_b16 v[174:175], v193 offset:49152
	s_waitcnt lgkmcnt(11)
	v_mfma_f32_16x16x32_bf16 v[80:83], v[168:171], v[214:217], v[80:83]
	v_mfma_f32_16x16x32_bf16 v[68:71], v[176:179], v[214:217], v[68:71]
	ds_read_b128 v[214:217], v207 offset:33792
	s_waitcnt lgkmcnt(11)
	v_mfma_f32_16x16x32_bf16 v[48:51], v[168:171], v[224:227], v[48:51]
	v_mfma_f32_16x16x32_bf16 v[44:47], v[176:179], v[224:227], v[44:47]
	ds_read_b128 v[224:227], v207 offset:35840
	s_waitcnt lgkmcnt(11)
	v_mfma_f32_16x16x32_bf16 v[32:35], v[168:171], v[232:235], v[32:35]
	v_mfma_f32_16x16x32_bf16 v[28:31], v[176:179], v[232:235], v[28:31]
	ds_read_b128 v[232:235], v207 offset:37888
	s_waitcnt lgkmcnt(11)
	v_mfma_f32_16x16x32_bf16 v[16:19], v[168:171], v[240:243], v[16:19]
	v_mfma_f32_16x16x32_bf16 v[12:15], v[176:179], v[240:243], v[12:15]
	ds_read_b128 v[240:243], v207 offset:39936
	ds_read_b64_tr_b16 v[168:169], v190 offset:57344
	ds_read_b64_tr_b16 v[170:171], v191 offset:57344
	ds_read_b64_tr_b16 v[176:177], v192 offset:57344
	ds_read_b64_tr_b16 v[178:179], v193 offset:57344
	s_waitcnt lgkmcnt(8)
	v_mfma_f32_16x16x32_bf16 v[144:147], v[164:167], v[210:213], v[144:147]
	v_mfma_f32_16x16x32_bf16 v[140:143], v[172:175], v[210:213], v[140:143]
	ds_read_b128 v[210:213], v207 offset:49152
	v_mfma_f32_16x16x32_bf16 v[128:131], v[164:167], v[218:221], v[128:131]
	v_mfma_f32_16x16x32_bf16 v[124:127], v[172:175], v[218:221], v[124:127]
	ds_read_b128 v[218:221], v207 offset:51200
	v_mfma_f32_16x16x32_bf16 v[112:115], v[164:167], v[228:231], v[112:115]
	v_mfma_f32_16x16x32_bf16 v[108:111], v[172:175], v[228:231], v[108:111]
	ds_read_b128 v[228:231], v207 offset:53248
	v_mfma_f32_16x16x32_bf16 v[104:107], v[164:167], v[236:239], v[104:107]
	v_mfma_f32_16x16x32_bf16 v[100:103], v[172:175], v[236:239], v[100:103]
	ds_read_b128 v[236:239], v207 offset:55296
	s_waitcnt lgkmcnt(4)
	v_mfma_f32_16x16x32_bf16 v[144:147], v[168:171], v[214:217], v[144:147]
	v_mfma_f32_16x16x32_bf16 v[140:143], v[176:179], v[214:217], v[140:143]
	ds_read_b128 v[214:217], v207 offset:50176
	v_mfma_f32_16x16x32_bf16 v[128:131], v[168:171], v[224:227], v[128:131]
	v_mfma_f32_16x16x32_bf16 v[124:127], v[176:179], v[224:227], v[124:127]
	ds_read_b128 v[224:227], v207 offset:52224
	v_mfma_f32_16x16x32_bf16 v[112:115], v[168:171], v[232:235], v[112:115]
	v_mfma_f32_16x16x32_bf16 v[108:111], v[176:179], v[232:235], v[108:111]
	ds_read_b128 v[232:235], v207 offset:54272
	v_mfma_f32_16x16x32_bf16 v[104:107], v[168:171], v[240:243], v[104:107]
	v_mfma_f32_16x16x32_bf16 v[100:103], v[176:179], v[240:243], v[100:103]
	ds_read_b128 v[240:243], v207 offset:56320
	s_waitcnt lgkmcnt(7)
	v_mfma_f32_16x16x32_bf16 v[56:59], v[164:167], v[210:213], v[56:59]
	v_mfma_f32_16x16x32_bf16 v[52:55], v[172:175], v[210:213], v[52:55]
	s_waitcnt vmcnt(9)
	v_cvt_pk_bf16_f32 v244, v64, v65
	v_cvt_pk_bf16_f32 v245, v66, v67
	ds_write_b64 v196, v[244:245] offset:16384
	global_load_dwordx4 v[64:67], v189, s[2:3]
	s_waitcnt lgkmcnt(7)
	v_mfma_f32_16x16x32_bf16 v[40:43], v[164:167], v[218:221], v[40:43]
	v_mfma_f32_16x16x32_bf16 v[36:39], v[172:175], v[218:221], v[36:39]
	s_waitcnt vmcnt(9)
	v_cvt_pk_bf16_f32 v244, v60, v61
	v_cvt_pk_bf16_f32 v245, v62, v63
	ds_write_b64 v197, v[244:245] offset:16384
	global_load_dwordx4 v[60:63], v189, s[48:49]
	s_waitcnt lgkmcnt(7)
	v_mfma_f32_16x16x32_bf16 v[24:27], v[164:167], v[228:231], v[24:27]
	v_mfma_f32_16x16x32_bf16 v[20:23], v[172:175], v[228:231], v[20:23]
	s_waitcnt vmcnt(9)
	v_cvt_pk_bf16_f32 v244, v76, v77
	v_cvt_pk_bf16_f32 v245, v78, v79
	ds_write_b64 v195, v[244:245] offset:16384
	s_add_u32 s98, s2, 0x4000
	s_addc_u32 s99, s3, 0
	global_load_dwordx4 v[76:79], v189, s[98:99]
	s_waitcnt lgkmcnt(7)
	v_mfma_f32_16x16x32_bf16 v[8:11], v[164:167], v[236:239], v[8:11]
	v_mfma_f32_16x16x32_bf16 v[2:5], v[172:175], v[236:239], v[4:7]
	s_waitcnt vmcnt(9)
	v_cvt_pk_bf16_f32 v244, v72, v73
	v_cvt_pk_bf16_f32 v245, v74, v75
	ds_write_b64 v197, v[244:245]
	s_add_u32 s100, s48, 0x4000
	s_addc_u32 s101, s49, 0
	global_load_dwordx4 v[72:75], v189, s[100:101]
	s_waitcnt lgkmcnt(7)
	v_mfma_f32_16x16x32_bf16 v[56:59], v[168:171], v[214:217], v[56:59]
	v_mfma_f32_16x16x32_bf16 v[52:55], v[176:179], v[214:217], v[52:55]
	s_waitcnt vmcnt(9)
	v_cvt_pk_bf16_f32 v244, v88, v89
	v_cvt_pk_bf16_f32 v245, v90, v91
	ds_write_b64 v194, v[244:245] offset:16384
	s_add_u32 s98, s2, 0x8000
	s_addc_u32 s99, s3, 0
	global_load_dwordx4 v[88:91], v189, s[98:99]
	s_waitcnt lgkmcnt(7)
	v_mfma_f32_16x16x32_bf16 v[40:43], v[168:171], v[224:227], v[40:43]
	v_mfma_f32_16x16x32_bf16 v[36:39], v[176:179], v[224:227], v[36:39]
	s_waitcnt vmcnt(9)
	v_cvt_pk_bf16_f32 v244, v84, v85
	v_cvt_pk_bf16_f32 v245, v86, v87
	ds_write_b64 v196, v[244:245]
	s_add_u32 s100, s48, 0x8000
	s_addc_u32 s101, s49, 0
	global_load_dwordx4 v[84:87], v189, s[100:101]
	s_waitcnt lgkmcnt(7)
	v_mfma_f32_16x16x32_bf16 v[24:27], v[168:171], v[232:235], v[24:27]
	v_mfma_f32_16x16x32_bf16 v[20:23], v[176:179], v[232:235], v[20:23]
	s_waitcnt vmcnt(9)
	v_cvt_pk_bf16_f32 v244, v96, v97
	v_cvt_pk_bf16_f32 v245, v98, v99
	ds_write_b64 v194, v[244:245]
	s_add_u32 s98, s2, 0xc000
	s_addc_u32 s99, s3, 0
	global_load_dwordx4 v[96:99], v189, s[98:99]
	s_waitcnt lgkmcnt(7)
	v_mfma_f32_16x16x32_bf16 v[8:11], v[168:171], v[240:243], v[8:11]
	v_mfma_f32_16x16x32_bf16 v[4:7], v[176:179], v[240:243], v[2:5]
	s_waitcnt vmcnt(9)
	v_cvt_pk_bf16_f32 v244, v92, v93
	v_cvt_pk_bf16_f32 v245, v94, v95
	ds_write_b64 v195, v[244:245]
	s_add_u32 s100, s48, 0xc000
	s_addc_u32 s101, s49, 0
	global_load_dwordx4 v[92:95], v189, s[100:101]
	s_setprio 0
.LBB0_868:
.Lswp_dnO_tail:
	s_add_i32 m0, s21, 0x8000
	s_waitcnt vmcnt(8)
	s_waitcnt lgkmcnt(0)
	s_barrier
	s_cmp_gt_u32 s34, 13
	s_cbranch_scc1 .LBB0_870
	global_load_lds_dwordx4 v[250:251], off
	s_add_i32 m0, s21, 0xa000
	s_mov_b32 s35, s34
	global_load_lds_dwordx4 v[252:253], off
	s_add_i32 s34, s35, 2
	s_mov_b32 s48, s34
	s_ashr_i32 s49, s48, 31
	s_mov_b64 s[50:51], s[94:95]
	v_cndmask_b32_e64 v1, 0, 1, s[0:1]
	v_cmp_ne_u32_e64 s[2:3], 1, v1
	s_andn2_b64 vcc, exec, s[0:1]
	s_cbranch_vccnz .LBB0_858
	v_lshl_add_u64 v[164:165], s[50:51], 0, v[184:185]
	s_add_i32 m0, s21, 0xc000
	v_lshl_add_u64 v[2:3], s[50:51], 0, v[186:187]
	global_load_lds_dwordx4 v[164:165], off
	s_add_i32 m0, s21, 0xe000
	s_nop 0
	global_load_lds_dwordx4 v[2:3], off
	s_branch .LBB0_858

.Lswp_dnO_half:
	ds_read_b64_tr_b16 v[164:165], v190 offset:32768
	ds_read_b64_tr_b16 v[166:167], v191 offset:32768
	ds_read_b64_tr_b16 v[172:173], v192 offset:32768
	ds_read_b64_tr_b16 v[174:175], v193 offset:32768
	ds_read_b128 v[210:213], v207 offset:32768
	ds_read_b128 v[218:221], v207 offset:34816
	ds_read_b128 v[228:231], v207 offset:36864
	ds_read_b128 v[236:239], v207 offset:38912
	ds_read_b64_tr_b16 v[168:169], v190 offset:40960
	ds_read_b64_tr_b16 v[170:171], v191 offset:40960
	ds_read_b64_tr_b16 v[176:177], v192 offset:40960
	ds_read_b64_tr_b16 v[178:179], v193 offset:40960
	ds_read_b128 v[214:217], v207 offset:33792
	ds_read_b128 v[224:227], v207 offset:35840
	ds_read_b128 v[232:235], v207 offset:37888
	ds_read_b128 v[240:243], v207 offset:39936
	s_lshl_b64 s[2:3], s[48:49], 19
	s_add_u32 s48, s2, 0x80000
	s_addc_u32 s49, s3, 0
	s_add_u32 s2, s74, s48
	s_addc_u32 s3, s43, s49
	s_add_u32 s48, s37, s48
	s_addc_u32 s49, s35, s49
	s_add_i32 s94, s34, 2
	s_ashr_i32 s95, s94, 31
	s_lshl_b64 s[94:95], s[94:95], 7
	s_add_u32 s94, s22, s94
	s_addc_u32 s95, s23, s95
	s_add_u32 s94, s94, 0x80
	s_addc_u32 s95, s95, 0
	v_lshl_add_u64 v[250:251], s[94:95], 0, v[180:181]
	v_lshl_add_u64 v[252:253], s[94:95], 0, v[182:183]
	s_setprio 1
	s_waitcnt lgkmcnt(11)
	v_mfma_f32_16x16x32_bf16 v[160:163], v[164:167], v[210:213], v[160:163]
	v_mfma_f32_16x16x32_bf16 v[156:159], v[172:175], v[210:213], v[156:159]
	ds_read_b128 v[210:213], v207 offset:32768
	s_waitcnt lgkmcnt(11)
	v_mfma_f32_16x16x32_bf16 v[152:155], v[164:167], v[218:221], v[152:155]
	v_mfma_f32_16x16x32_bf16 v[148:151], v[172:175], v[218:221], v[148:151]
	ds_read_b128 v[218:221], v207 offset:34816
	s_waitcnt lgkmcnt(11)
	v_mfma_f32_16x16x32_bf16 v[136:139], v[164:167], v[228:231], v[136:139]
	v_mfma_f32_16x16x32_bf16 v[132:135], v[172:175], v[228:231], v[132:135]
	ds_read_b128 v[228:231], v207 offset:36864
	s_waitcnt lgkmcnt(11)
	v_mfma_f32_16x16x32_bf16 v[120:123], v[164:167], v[236:239], v[120:123]
	v_mfma_f32_16x16x32_bf16 v[116:119], v[172:175], v[236:239], v[116:119]
	ds_read_b128 v[236:239], v207 offset:38912
	ds_read_b64_tr_b16 v[164:165], v190 offset:49152
	ds_read_b64_tr_b16 v[166:167], v191 offset:49152
	ds_read_b64_tr_b16 v[172:173], v192 offset:49152
	ds_read_b64_tr_b16 v[174:175], v193 offset:49152
	s_waitcnt lgkmcnt(11)
	v_mfma_f32_16x16x32_bf16 v[160:163], v[168:171], v[214:217], v[160:163]
	v_mfma_f32_16x16x32_bf16 v[156:159], v[176:179], v[214:217], v[156:159]
	ds_read_b128 v[214:217], v207 offset:33792
	s_waitcnt lgkmcnt(11)
	v_mfma_f32_16x16x32_bf16 v[152:155], v[168:171], v[224:227], v[152:155]
	v_mfma_f32_16x16x32_bf16 v[148:151], v[176:179], v[224:227], v[148:151]
	ds_read_b128 v[224:227], v207 offset:35840
	s_waitcnt lgkmcnt(11)
	v_mfma_f32_16x16x32_bf16 v[136:139], v[168:171], v[232:235], v[136:139]
	v_mfma_f32_16x16x32_bf16 v[132:135], v[176:179], v[232:235], v[132:135]
	ds_read_b128 v[232:235], v207 offset:37888
	s_waitcnt lgkmcnt(11)
	v_mfma_f32_16x16x32_bf16 v[120:123], v[168:171], v[240:243], v[120:123]
	v_mfma_f32_16x16x32_bf16 v[116:119], v[176:179], v[240:243], v[116:119]
	ds_read_b128 v[240:243], v207 offset:39936
	ds_read_b64_tr_b16 v[168:169], v190 offset:57344
	ds_read_b64_tr_b16 v[170:171], v191 offset:57344
	ds_read_b64_tr_b16 v[176:177], v192 offset:57344
	ds_read_b64_tr_b16 v[178:179], v193 offset:57344
	s_waitcnt lgkmcnt(8)
	v_mfma_f32_16x16x32_bf16 v[144:147], v[164:167], v[210:213], v[144:147]
	v_mfma_f32_16x16x32_bf16 v[140:143], v[172:175], v[210:213], v[140:143]
	s_waitcnt vmcnt(9)
	v_cvt_pk_bf16_f32 v244, v64, v65
	v_cvt_pk_bf16_f32 v245, v66, v67
	ds_write_b64 v196, v[244:245] offset:16384
	global_load_dwordx4 v[64:67], v189, s[2:3]
	v_mfma_f32_16x16x32_bf16 v[128:131], v[164:167], v[218:221], v[128:131]
	v_mfma_f32_16x16x32_bf16 v[124:127], v[172:175], v[218:221], v[124:127]
	s_waitcnt vmcnt(9)
	v_cvt_pk_bf16_f32 v244, v60, v61
	v_cvt_pk_bf16_f32 v245, v62, v63
	ds_write_b64 v197, v[244:245] offset:16384
	global_load_dwordx4 v[60:63], v189, s[48:49]
	v_mfma_f32_16x16x32_bf16 v[112:115], v[164:167], v[228:231], v[112:115]
	v_mfma_f32_16x16x32_bf16 v[108:111], v[172:175], v[228:231], v[108:111]
	s_waitcnt vmcnt(9)
	v_cvt_pk_bf16_f32 v244, v76, v77
	v_cvt_pk_bf16_f32 v245, v78, v79
	ds_write_b64 v195, v[244:245] offset:16384
	s_add_u32 s98, s2, 0x4000
	s_addc_u32 s99, s3, 0
	global_load_dwordx4 v[76:79], v189, s[98:99]
	v_mfma_f32_16x16x32_bf16 v[104:107], v[164:167], v[236:239], v[104:107]
	v_mfma_f32_16x16x32_bf16 v[100:103], v[172:175], v[236:239], v[100:103]
	s_waitcnt vmcnt(9)
	v_cvt_pk_bf16_f32 v244, v72, v73
	v_cvt_pk_bf16_f32 v245, v74, v75
	ds_write_b64 v197, v[244:245]
	s_add_u32 s100, s48, 0x4000
	s_addc_u32 s101, s49, 0
	global_load_dwordx4 v[72:75], v189, s[100:101]
	s_waitcnt lgkmcnt(4)
	v_mfma_f32_16x16x32_bf16 v[144:147], v[168:171], v[214:217], v[144:147]
	v_mfma_f32_16x16x32_bf16 v[140:143], v[176:179], v[214:217], v[140:143]
	s_waitcnt vmcnt(9)
	v_cvt_pk_bf16_f32 v244, v88, v89
	v_cvt_pk_bf16_f32 v245, v90, v91
	ds_write_b64 v194, v[244:245] offset:16384
	s_add_u32 s98, s2, 0x8000
	s_addc_u32 s99, s3, 0
	global_load_dwordx4 v[88:91], v189, s[98:99]
	v_mfma_f32_16x16x32_bf16 v[128:131], v[168:171], v[224:227], v[128:131]
	v_mfma_f32_16x16x32_bf16 v[124:127], v[176:179], v[224:227], v[124:127]
	s_waitcnt vmcnt(9)
	v_cvt_pk_bf16_f32 v244, v84, v85
	v_cvt_pk_bf16_f32 v245, v86, v87
	ds_write_b64 v196, v[244:245]
	s_add_u32 s100, s48, 0x8000
	s_addc_u32 s101, s49, 0
	global_load_dwordx4 v[84:87], v189, s[100:101]
	v_mfma_f32_16x16x32_bf16 v[112:115], v[168:171], v[232:235], v[112:115]
	v_mfma_f32_16x16x32_bf16 v[108:111], v[176:179], v[232:235], v[108:111]
	s_waitcnt vmcnt(9)
	v_cvt_pk_bf16_f32 v244, v96, v97
	v_cvt_pk_bf16_f32 v245, v98, v99
	ds_write_b64 v194, v[244:245]
	s_add_u32 s98, s2, 0xc000
	s_addc_u32 s99, s3, 0
	global_load_dwordx4 v[96:99], v189, s[98:99]
	v_mfma_f32_16x16x32_bf16 v[104:107], v[168:171], v[240:243], v[104:107]
	v_mfma_f32_16x16x32_bf16 v[100:103], v[176:179], v[240:243], v[100:103]
	s_waitcnt vmcnt(9)
	v_cvt_pk_bf16_f32 v244, v92, v93
	v_cvt_pk_bf16_f32 v245, v94, v95
	ds_write_b64 v195, v[244:245]
	s_add_u32 s100, s48, 0xc000
	s_addc_u32 s101, s49, 0
	global_load_dwordx4 v[92:95], v189, s[100:101]
	s_setprio 0
	s_branch .Lswp_dnO_tail
